# baseline (speedup 1.0000x reference)
.LBB1_23:
	s_add_u32 s0, s8, 0x3700000
	s_addc_u32 s1, s9, 0
	s_cmpk_gt_u32 s3, 0x17f
	s_mov_b64 s[6:7], -1
	s_cbranch_scc0 .LBB1_29
	s_cmpk_gt_u32 s3, 0x18f
	s_cbranch_scc0 .LBB1_26
	v_mov_b32_e32 v1, v0
	s_add_i32 s6, 0, 0x20000
	v_lshrrev_b32_e32 v131, 1, v1
	v_and_b32_e32 v130, 15, v1
	v_and_b32_e32 v131, 0x60, v131
	v_lshlrev_b32_e32 v132, 2, v131
	v_lshlrev_b32_e32 v133, 2, v130
	v_add3_u32 v134, s6, v132, v133
	v_lshlrev_b32_e32 v132, 1, v1
	v_and_b32_e32 v135, 32, v132
	ds_read2_b32 v[132:133], v134 offset1:16
	v_mov_b32_e32 v138, 0
	v_mov_b32_e32 v141, 0
	v_or_b32_e32 v130, v131, v130
	v_ashrrev_i32_e32 v131, 2, v1
	s_waitcnt lgkmcnt(0)
	v_add_f32_e32 v136, v132, v126
	v_add_f32_e32 v137, v132, v127
	v_cvt_pk_fp8_f32 v138, v136, v137
	v_add_f32_e32 v139, v132, v122
	v_add_f32_e32 v140, v132, v123
	v_cvt_pk_fp8_f32 v141, v139, v140
	v_add_f32_e32 v136, v132, v128
	v_add_f32_e32 v137, v132, v129
	v_cvt_pk_fp8_f32 v138, v136, v137 op_sel:[0,0,1]
	v_add_f32_e32 v136, v132, v124
	v_add_f32_e32 v137, v132, v125
	v_and_b32_e32 v131, 0xffffffc0, v131
	v_cvt_pk_fp8_f32 v141, v136, v137 op_sel:[0,0,1]
	v_add3_u32 v131, 0, v131, v135
	v_lshrrev_b32_e32 v135, 3, v1
	v_and_b32_e32 v135, 4, v135
	v_mul_u32_u24_e32 v130, 0x90, v130
	v_add3_u32 v130, v131, v135, v130
	v_add_f32_e32 v135, v132, v118
	v_add_f32_e32 v136, v132, v119
	v_mov_b32_e32 v137, 0
	ds_write2_b32 v130, v138, v141 offset1:2
	v_cvt_pk_fp8_f32 v137, v135, v136
	v_add_f32_e32 v138, v132, v114
	v_add_f32_e32 v139, v132, v115
	v_mov_b32_e32 v140, 0
	v_cvt_pk_fp8_f32 v140, v138, v139
	v_add_f32_e32 v135, v132, v120
	v_add_f32_e32 v136, v132, v121
	v_cvt_pk_fp8_f32 v137, v135, v136 op_sel:[0,0,1]
	v_add_f32_e32 v135, v132, v116
	v_add_f32_e32 v136, v132, v117
	v_cvt_pk_fp8_f32 v140, v135, v136 op_sel:[0,0,1]
	v_add_f32_e32 v135, v132, v62
	v_add_f32_e32 v136, v132, v63
	v_mov_b32_e32 v138, 0
	v_cvt_pk_fp8_f32 v138, v135, v136
	v_add_f32_e32 v139, v132, v58
	v_add_f32_e32 v141, v132, v59
	v_mov_b32_e32 v142, 0
	v_cvt_pk_fp8_f32 v142, v139, v141
	v_add_f32_e32 v135, v132, v64
	v_add_f32_e32 v136, v132, v65
	v_cvt_pk_fp8_f32 v138, v135, v136 op_sel:[0,0,1]
	v_add_f32_e32 v135, v132, v60
	v_add_f32_e32 v136, v132, v61
	v_cvt_pk_fp8_f32 v142, v135, v136 op_sel:[0,0,1]
	v_add_f32_e32 v135, v132, v54
	v_add_f32_e32 v136, v132, v55
	v_mov_b32_e32 v139, 0
	v_cvt_pk_fp8_f32 v139, v135, v136
	v_add_f32_e32 v141, v132, v50
	v_add_f32_e32 v143, v132, v51
	v_mov_b32_e32 v144, 0
	v_cvt_pk_fp8_f32 v144, v141, v143
	v_add_f32_e32 v135, v132, v56
	v_add_f32_e32 v136, v132, v57
	v_cvt_pk_fp8_f32 v139, v135, v136 op_sel:[0,0,1]
	v_add_f32_e32 v135, v132, v52
	v_add_f32_e32 v132, v132, v53
	v_cvt_pk_fp8_f32 v144, v135, v132 op_sel:[0,0,1]
	v_add_u32_e32 v132, 0x9000, v130
	ds_write2_b32 v130, v137, v140 offset0:4 offset1:6
	ds_write2_b32 v132, v138, v142 offset1:2
	ds_write2_b32 v132, v139, v144 offset0:4 offset1:6
	v_add_f32_e32 v132, v133, v102
	v_add_f32_e32 v135, v133, v103
	v_mov_b32_e32 v136, 0
	v_cvt_pk_fp8_f32 v136, v132, v135
	v_add_f32_e32 v137, v133, v98
	v_add_f32_e32 v138, v133, v99
	v_mov_b32_e32 v139, 0
	v_cvt_pk_fp8_f32 v139, v137, v138
	v_add_f32_e32 v132, v133, v104
	v_add_f32_e32 v135, v133, v105
	v_cvt_pk_fp8_f32 v136, v132, v135 op_sel:[0,0,1]
	v_add_f32_e32 v132, v133, v100
	v_add_f32_e32 v135, v133, v101
	v_cvt_pk_fp8_f32 v139, v132, v135 op_sel:[0,0,1]
	v_add_f32_e32 v135, v133, v94
	v_add_f32_e32 v137, v133, v95
	v_mov_b32_e32 v138, 0
	v_cvt_pk_fp8_f32 v138, v135, v137
	v_add_f32_e32 v140, v133, v90
	v_add_f32_e32 v141, v133, v91
	v_mov_b32_e32 v142, 0
	v_cvt_pk_fp8_f32 v142, v140, v141
	v_add_f32_e32 v135, v133, v96
	v_add_f32_e32 v137, v133, v97
	v_cvt_pk_fp8_f32 v138, v135, v137 op_sel:[0,0,1]
	v_add_f32_e32 v135, v133, v92
	v_add_f32_e32 v137, v133, v93
	v_cvt_pk_fp8_f32 v142, v135, v137 op_sel:[0,0,1]
	v_add_f32_e32 v135, v133, v46
	v_add_f32_e32 v137, v133, v47
	v_mov_b32_e32 v140, 0
	v_cvt_pk_fp8_f32 v140, v135, v137
	v_add_f32_e32 v141, v133, v42
	v_add_f32_e32 v143, v133, v43
	v_mov_b32_e32 v144, 0
	v_cvt_pk_fp8_f32 v144, v141, v143
	v_add_f32_e32 v135, v133, v48
	v_add_f32_e32 v137, v133, v49
	v_cvt_pk_fp8_f32 v140, v135, v137 op_sel:[0,0,1]
	v_add_f32_e32 v135, v133, v44
	v_add_f32_e32 v137, v133, v45
	v_cvt_pk_fp8_f32 v144, v135, v137 op_sel:[0,0,1]
	v_add_u32_e32 v132, 0x800, v130
	ds_write2_b32 v132, v136, v139 offset0:64 offset1:66
	ds_write2_b32 v132, v138, v142 offset0:68 offset1:70
	v_add_u32_e32 v132, 0x9800, v130
	v_add_f32_e32 v135, v133, v38
	v_add_f32_e32 v136, v133, v39
	v_mov_b32_e32 v137, 0
	ds_write2_b32 v132, v140, v144 offset0:64 offset1:66
	v_cvt_pk_fp8_f32 v137, v135, v136
	v_add_f32_e32 v135, v133, v34
	v_add_f32_e32 v139, v133, v35
	v_mov_b32_e32 v140, 0
	v_cvt_pk_fp8_f32 v140, v135, v139
	ds_read2_b32 v[134:135], v134 offset0:128 offset1:144
	v_add_f32_e32 v136, v133, v40
	v_add_f32_e32 v138, v133, v41
	v_cvt_pk_fp8_f32 v137, v136, v138 op_sel:[0,0,1]
	v_add_f32_e32 v136, v133, v36
	v_add_f32_e32 v133, v133, v37
	v_cvt_pk_fp8_f32 v140, v136, v133 op_sel:[0,0,1]
	s_waitcnt lgkmcnt(0)
	v_add_f32_e32 v133, v134, v110
	v_add_f32_e32 v136, v134, v111
	v_mov_b32_e32 v138, 0
	v_cvt_pk_fp8_f32 v138, v133, v136
	v_add_f32_e32 v139, v134, v106
	v_add_f32_e32 v141, v134, v107
	v_mov_b32_e32 v142, 0
	v_cvt_pk_fp8_f32 v142, v139, v141
	v_add_f32_e32 v133, v134, v112
	v_add_f32_e32 v136, v134, v113
	v_cvt_pk_fp8_f32 v138, v133, v136 op_sel:[0,0,1]
	v_add_f32_e32 v133, v134, v108
	v_add_f32_e32 v136, v134, v109
	v_cvt_pk_fp8_f32 v142, v133, v136 op_sel:[0,0,1]
	v_add_f32_e32 v133, v134, v86
	v_add_f32_e32 v136, v134, v87
	v_mov_b32_e32 v139, 0
	v_cvt_pk_fp8_f32 v139, v133, v136
	v_add_f32_e32 v141, v134, v82
	v_add_f32_e32 v143, v134, v83
	v_mov_b32_e32 v144, 0
	v_cvt_pk_fp8_f32 v144, v141, v143
	v_add_f32_e32 v133, v134, v88
	v_add_f32_e32 v136, v134, v89
	v_cvt_pk_fp8_f32 v139, v133, v136 op_sel:[0,0,1]
	v_add_f32_e32 v133, v134, v84
	v_add_f32_e32 v136, v134, v85
	v_cvt_pk_fp8_f32 v144, v133, v136 op_sel:[0,0,1]
	ds_write2_b32 v132, v137, v140 offset0:68 offset1:70
	v_add_u32_e32 v132, 0x4800, v130
	ds_write2_b32 v132, v138, v142 offset1:2
	ds_write2_b32 v132, v139, v144 offset0:4 offset1:6
	v_add_f32_e32 v132, v134, v30
	v_add_f32_e32 v133, v134, v31
	v_mov_b32_e32 v136, 0
	v_cvt_pk_fp8_f32 v136, v132, v133
	v_add_f32_e32 v137, v134, v26
	v_add_f32_e32 v138, v134, v27
	v_mov_b32_e32 v139, 0
	v_cvt_pk_fp8_f32 v139, v137, v138
	v_add_f32_e32 v132, v134, v32
	v_add_f32_e32 v133, v134, v33
	v_cvt_pk_fp8_f32 v136, v132, v133 op_sel:[0,0,1]
	v_add_f32_e32 v132, v134, v28
	v_add_f32_e32 v133, v134, v29
	v_cvt_pk_fp8_f32 v139, v132, v133 op_sel:[0,0,1]
	v_add_f32_e32 v133, v134, v22
	v_add_f32_e32 v137, v134, v23
	v_mov_b32_e32 v138, 0
	v_cvt_pk_fp8_f32 v138, v133, v137
	v_add_f32_e32 v140, v134, v14
	v_add_f32_e32 v141, v134, v15
	v_mov_b32_e32 v142, 0
	v_cvt_pk_fp8_f32 v142, v140, v141
	v_add_f32_e32 v133, v134, v24
	v_add_f32_e32 v137, v134, v25
	v_cvt_pk_fp8_f32 v138, v133, v137 op_sel:[0,0,1]
	v_add_f32_e32 v133, v134, v16
	v_add_f32_e32 v134, v134, v17
	v_cvt_pk_fp8_f32 v142, v133, v134 op_sel:[0,0,1]
	v_add_f32_e32 v133, v135, v78
	v_add_f32_e32 v134, v135, v79
	v_mov_b32_e32 v137, 0
	v_cvt_pk_fp8_f32 v137, v133, v134
	v_add_f32_e32 v140, v135, v74
	v_add_f32_e32 v141, v135, v75
	v_mov_b32_e32 v143, 0
	v_cvt_pk_fp8_f32 v143, v140, v141
	v_add_f32_e32 v133, v135, v80
	v_add_f32_e32 v134, v135, v81
	v_cvt_pk_fp8_f32 v137, v133, v134 op_sel:[0,0,1]
	v_add_f32_e32 v133, v135, v76
	v_add_f32_e32 v134, v135, v77
	v_cvt_pk_fp8_f32 v143, v133, v134 op_sel:[0,0,1]
	v_add_u32_e32 v132, 0xd800, v130
	ds_write2_b32 v132, v136, v139 offset1:2
	ds_write2_b32 v132, v138, v142 offset0:4 offset1:6
	v_add_u32_e32 v132, 0x5000, v130
	v_add_f32_e32 v133, v135, v70
	v_add_f32_e32 v134, v135, v71
	v_mov_b32_e32 v136, 0
	ds_write2_b32 v132, v137, v143 offset0:64 offset1:66
	v_cvt_pk_fp8_f32 v136, v133, v134
	v_add_f32_e32 v137, v135, v66
	v_add_f32_e32 v138, v135, v67
	v_mov_b32_e32 v139, 0
	v_cvt_pk_fp8_f32 v139, v137, v138
	v_add_f32_e32 v133, v135, v72
	v_add_f32_e32 v134, v135, v73
	v_cvt_pk_fp8_f32 v136, v133, v134 op_sel:[0,0,1]
	v_add_f32_e32 v133, v135, v68
	v_add_f32_e32 v134, v135, v69
	v_cvt_pk_fp8_f32 v139, v133, v134 op_sel:[0,0,1]
	v_add_f32_e32 v133, v135, v10
	v_add_f32_e32 v134, v135, v11
	v_mov_b32_e32 v137, 0
	v_cvt_pk_fp8_f32 v137, v133, v134
	v_add_f32_e32 v138, v135, v6
	v_add_f32_e32 v140, v135, v7
	v_mov_b32_e32 v141, 0
	v_cvt_pk_fp8_f32 v141, v138, v140
	v_add_f32_e32 v133, v135, v12
	v_add_f32_e32 v134, v135, v13
	v_cvt_pk_fp8_f32 v137, v133, v134 op_sel:[0,0,1]
	v_add_f32_e32 v133, v135, v8
	v_add_f32_e32 v134, v135, v9
	v_cvt_pk_fp8_f32 v141, v133, v134 op_sel:[0,0,1]
	v_add_f32_e32 v133, v135, v2
	v_add_f32_e32 v134, v135, v3
	v_mov_b32_e32 v138, 0
	v_cvt_pk_fp8_f32 v138, v133, v134
	v_add_f32_e32 v140, v135, v18
	v_add_f32_e32 v142, v135, v19
	v_mov_b32_e32 v143, 0
	v_cvt_pk_fp8_f32 v143, v140, v142
	v_add_f32_e32 v133, v135, v4
	v_add_f32_e32 v134, v135, v5
	v_cvt_pk_fp8_f32 v138, v133, v134 op_sel:[0,0,1]
	v_add_f32_e32 v133, v135, v20
	v_add_f32_e32 v134, v135, v21
	v_cvt_pk_fp8_f32 v143, v133, v134 op_sel:[0,0,1]
	v_add_u32_e32 v130, 0xe000, v130
	s_and_b32 s7, s3, 0x7ffffffe
	ds_write2_b32 v132, v136, v139 offset0:68 offset1:70
	ds_write2_b32 v130, v137, v141 offset0:64 offset1:66
	ds_write2_b32 v130, v138, v143 offset0:68 offset1:70
	v_lshlrev_b32_e32 v130, 4, v1
	s_add_i32 s12, s7, 0xfffffe70
	v_and_b32_e32 v130, 0x70, v130
	s_lshl_b32 s7, s3, 2
	v_ashrrev_i32_e32 v136, 3, v1
	v_ashrrev_i32_e32 v134, 11, v1
	s_movk_i32 s6, 0x90
	v_mov_b32_e32 v131, 0
	v_add_u32_e32 v138, 0, v130
	s_and_b32 s13, s7, 4
	v_add_lshl_u32 v134, s12, v134, 3
	v_bfe_u32 v135, v136, 6, 2
	v_lshl_add_u64 v[140:141], s[0:1], 0, v[130:131]
	v_mad_u64_u32 v[130:131], s[10:11], v136, s6, v[138:139]
	v_or3_b32 v134, v134, v135, s13
	s_waitcnt lgkmcnt(0)
	s_barrier
	ds_read_b128 v[130:133], v130
	v_ashrrev_i32_e32 v135, 31, v134
	v_lshlrev_b64 v[134:135], 6, v[134:135]
	v_and_or_b32 v134, v136, 63, v134
	s_movk_i32 s14, 0x480
	v_add_u32_e32 v139, 0x200, v1
	v_mad_u64_u32 v[142:143], s[10:11], v134, s14, v[140:141]
	v_ashrrev_i32_e32 v144, 3, v139
	v_mad_i32_i24 v143, v135, s14, v143
	v_mad_u64_u32 v[134:135], s[10:11], v144, s6, v[138:139]
	ds_read_b128 v[134:137], v134
	s_waitcnt lgkmcnt(1)
	global_store_dwordx4 v[142:143], v[130:133], off sc1
	s_nop 1
	v_ashrrev_i32_e32 v130, 11, v139
	v_add_lshl_u32 v130, s12, v130, 3
	v_bfe_u32 v131, v144, 6, 2
	v_or3_b32 v130, v130, v131, s13
	v_ashrrev_i32_e32 v131, 31, v130
	v_lshlrev_b64 v[130:131], 6, v[130:131]
	v_and_or_b32 v130, v144, 63, v130
	v_mad_u64_u32 v[132:133], s[10:11], v130, s14, v[140:141]
	v_mad_i32_i24 v133, v131, s14, v133
	s_waitcnt lgkmcnt(0)
	global_store_dwordx4 v[132:133], v[134:137], off sc1
	s_nop 1
	v_add_u32_e32 v134, 0x400, v1
	v_ashrrev_i32_e32 v136, 3, v134
	v_ashrrev_i32_e32 v134, 11, v134
	v_add_lshl_u32 v134, s12, v134, 3
	v_bfe_u32 v135, v136, 6, 2
	v_mad_u64_u32 v[130:131], s[10:11], v136, s6, v[138:139]
	v_or3_b32 v134, v134, v135, s13
	ds_read_b128 v[130:133], v130
	v_ashrrev_i32_e32 v135, 31, v134
	v_lshlrev_b64 v[134:135], 6, v[134:135]
	v_and_or_b32 v134, v136, 63, v134
	v_add_u32_e32 v139, 0x600, v1
	v_mad_u64_u32 v[142:143], s[10:11], v134, s14, v[140:141]
	v_ashrrev_i32_e32 v144, 3, v139
	v_mad_i32_i24 v143, v135, s14, v143
	v_mad_u64_u32 v[134:135], s[10:11], v144, s6, v[138:139]
	ds_read_b128 v[134:137], v134
	s_waitcnt lgkmcnt(1)
	global_store_dwordx4 v[142:143], v[130:133], off sc1
	s_nop 1
	v_ashrrev_i32_e32 v130, 11, v139
	v_add_lshl_u32 v130, s12, v130, 3
	v_bfe_u32 v131, v144, 6, 2
	v_or3_b32 v130, v130, v131, s13
	v_ashrrev_i32_e32 v131, 31, v130
	v_lshlrev_b64 v[130:131], 6, v[130:131]
	v_and_or_b32 v130, v144, 63, v130
	v_mad_u64_u32 v[132:133], s[10:11], v130, s14, v[140:141]
	v_mad_i32_i24 v133, v131, s14, v133
	s_waitcnt lgkmcnt(0)
	global_store_dwordx4 v[132:133], v[134:137], off sc1
	s_nop 1
	v_add_u32_e32 v134, 0x800, v1
	v_ashrrev_i32_e32 v136, 3, v134
	v_ashrrev_i32_e32 v134, 11, v134
	v_add_lshl_u32 v134, s12, v134, 3
	v_bfe_u32 v135, v136, 6, 2
	v_mad_u64_u32 v[130:131], s[10:11], v136, s6, v[138:139]
	v_or3_b32 v134, v134, v135, s13
	ds_read_b128 v[130:133], v130
	v_ashrrev_i32_e32 v135, 31, v134
	v_lshlrev_b64 v[134:135], 6, v[134:135]
	v_and_or_b32 v134, v136, 63, v134
	v_add_u32_e32 v139, 0xa00, v1
	v_mad_u64_u32 v[142:143], s[10:11], v134, s14, v[140:141]
	v_ashrrev_i32_e32 v144, 3, v139
	v_mad_i32_i24 v143, v135, s14, v143
	v_mad_u64_u32 v[134:135], s[10:11], v144, s6, v[138:139]
	ds_read_b128 v[134:137], v134
	s_waitcnt lgkmcnt(1)
	global_store_dwordx4 v[142:143], v[130:133], off sc1
	s_nop 1
	v_ashrrev_i32_e32 v130, 11, v139
	v_add_lshl_u32 v130, s12, v130, 3
	v_bfe_u32 v131, v144, 6, 2
	v_or3_b32 v130, v130, v131, s13
	v_ashrrev_i32_e32 v131, 31, v130
	v_lshlrev_b64 v[130:131], 6, v[130:131]
	v_and_or_b32 v130, v144, 63, v130
	v_mad_u64_u32 v[132:133], s[10:11], v130, s14, v[140:141]
	v_mad_i32_i24 v133, v131, s14, v133
	s_waitcnt lgkmcnt(0)
	global_store_dwordx4 v[132:133], v[134:137], off sc1
	s_nop 1
	v_add_u32_e32 v134, 0xc00, v1
	v_ashrrev_i32_e32 v136, 3, v134
	v_ashrrev_i32_e32 v134, 11, v134
	v_add_lshl_u32 v134, s12, v134, 3
	v_bfe_u32 v135, v136, 6, 2
	v_mad_u64_u32 v[130:131], s[10:11], v136, s6, v[138:139]
	v_or3_b32 v134, v134, v135, s13
	ds_read_b128 v[130:133], v130
	v_ashrrev_i32_e32 v135, 31, v134
	v_lshlrev_b64 v[134:135], 6, v[134:135]
	v_and_or_b32 v134, v136, 63, v134
	v_add_u32_e32 v1, 0xe00, v1
	v_mad_u64_u32 v[142:143], s[10:11], v134, s14, v[140:141]
	v_ashrrev_i32_e32 v139, 3, v1
	v_mad_i32_i24 v143, v135, s14, v143
	v_mad_u64_u32 v[134:135], s[6:7], v139, s6, v[138:139]
	v_ashrrev_i32_e32 v1, 11, v1
	ds_read_b128 v[134:137], v134
	s_waitcnt lgkmcnt(1)
	global_store_dwordx4 v[142:143], v[130:133], off sc1
	v_add_lshl_u32 v1, s12, v1, 3
	s_nop 0
	v_bfe_u32 v130, v139, 6, 2
	v_or3_b32 v130, v1, v130, s13
	v_ashrrev_i32_e32 v131, 31, v130
	v_lshlrev_b64 v[130:131], 6, v[130:131]
	v_and_or_b32 v1, v139, 63, v130
	v_mad_u64_u32 v[132:133], s[6:7], v1, s14, v[140:141]
	v_mad_i32_i24 v133, v131, s14, v133
	s_waitcnt lgkmcnt(0)
	global_store_dwordx4 v[132:133], v[134:137], off sc1
	s_mov_b64 s[6:7], 0
.LBB1_26:
	s_andn2_b64 vcc, exec, s[6:7]
	s_cbranch_vccnz .LBB1_28
	s_add_i32 s6, s3, 0xfffffe80
	v_mov_b32_e32 v1, v0
	s_lshr_b32 s6, s6, 1
	s_and_b32 s6, s6, 0x7ffffffc
	v_ashrrev_i32_e32 v130, 8, v1
	v_and_b32_e32 v134, 15, v1
	v_and_b32_e32 v132, 48, v1
	s_add_i32 s7, 0, 0x20000
	v_add_u32_e32 v160, s6, v130
	v_lshrrev_b32_e32 v135, 1, v1
	s_movk_i32 s6, 0x60
	v_and_b32_e32 v1, 0xffffff00, v1
	v_and_or_b32 v161, v135, s6, v134
	v_add3_u32 v1, s7, v132, v1
	s_lshl_b32 s6, s3, 4
	v_mov_b32_e32 v133, 0
	ds_read_b128 v[134:137], v1
	ds_read_b128 v[138:141], v1 offset:64
	ds_read_b128 v[142:145], v1 offset:128
	ds_read_b128 v[146:149], v1 offset:192
	s_and_b32 s7, s6, 0x70
	v_lshl_add_u64 v[130:131], s[4:5], 0, v[132:133]
	v_add_u32_e32 v132, s7, v160
	s_mov_b32 s6, 0x12000
	v_mad_i64_i32 v[158:159], s[10:11], v132, s6, v[130:131]
	s_waitcnt lgkmcnt(3)
	v_add_f32_e32 v132, v126, v134
	v_add_f32_e32 v151, v127, v135
	v_mov_b32_e32 v150, v133
	v_cvt_pk_fp8_f32 v150, v132, v151
	s_waitcnt lgkmcnt(2)
	v_add_f32_e32 v132, v122, v138
	v_add_f32_e32 v154, v123, v139
	v_mov_b32_e32 v151, v133
	v_cvt_pk_fp8_f32 v151, v132, v154
	v_add_f32_e32 v152, v128, v136
	v_add_f32_e32 v153, v129, v137
	v_cvt_pk_fp8_f32 v150, v152, v153 op_sel:[0,0,1]
	v_add_f32_e32 v132, v124, v140
	v_add_f32_e32 v152, v125, v141
	v_cvt_pk_fp8_f32 v151, v132, v152 op_sel:[0,0,1]
	s_waitcnt lgkmcnt(1)
	v_add_f32_e32 v132, v118, v142
	v_add_f32_e32 v153, v119, v143
	v_mov_b32_e32 v152, v133
	v_cvt_pk_fp8_f32 v152, v132, v153
	s_waitcnt lgkmcnt(0)
	v_add_f32_e32 v132, v114, v146
	v_add_f32_e32 v156, v115, v147
	v_mov_b32_e32 v153, v133
	v_cvt_pk_fp8_f32 v153, v132, v156
	v_add_f32_e32 v154, v120, v144
	v_add_f32_e32 v155, v121, v145
	v_cvt_pk_fp8_f32 v152, v154, v155 op_sel:[0,0,1]
	v_add_f32_e32 v132, v116, v148
	v_add_f32_e32 v154, v117, v149
	v_cvt_pk_fp8_f32 v153, v132, v154 op_sel:[0,0,1]
	v_add_f32_e32 v132, v102, v134
	v_add_f32_e32 v155, v103, v135
	v_mov_b32_e32 v154, v133
	v_cvt_pk_fp8_f32 v154, v132, v155
	v_add_f32_e32 v132, v98, v138
	v_add_f32_e32 v162, v99, v139
	v_mov_b32_e32 v155, v133
	v_cvt_pk_fp8_f32 v155, v132, v162
	v_add_f32_e32 v156, v104, v136
	v_add_f32_e32 v157, v105, v137
	v_cvt_pk_fp8_f32 v154, v156, v157 op_sel:[0,0,1]
	v_add_f32_e32 v132, v100, v140
	v_add_f32_e32 v156, v101, v141
	v_cvt_pk_fp8_f32 v155, v132, v156 op_sel:[0,0,1]
	v_add_f32_e32 v132, v94, v142
	v_add_f32_e32 v157, v95, v143
	v_mov_b32_e32 v156, v133
	v_cvt_pk_fp8_f32 v156, v132, v157
	v_add_f32_e32 v132, v90, v146
	v_add_f32_e32 v164, v91, v147
	v_mov_b32_e32 v157, v133
	v_cvt_pk_fp8_f32 v157, v132, v164
	v_add_f32_e32 v162, v96, v144
	v_add_f32_e32 v163, v97, v145
	v_cvt_pk_fp8_f32 v156, v162, v163 op_sel:[0,0,1]
	v_add_f32_e32 v132, v92, v148
	v_add_f32_e32 v162, v93, v149
	v_cvt_pk_fp8_f32 v157, v132, v162 op_sel:[0,0,1]
	v_lshlrev_b32_e32 v132, 6, v161
	v_lshl_add_u64 v[158:159], v[158:159], 0, v[132:133]
	global_store_dwordx4 v[158:159], v[150:153], off sc1
	global_store_dwordx4 v[158:159], v[154:157], off offset:1024 sc1
	v_add_f32_e32 v158, v83, v147
	v_add_f32_e32 v151, v110, v134
	v_add_f32_e32 v152, v111, v135
	v_mov_b32_e32 v150, v133
	v_cvt_pk_fp8_f32 v150, v151, v152
	v_add_f32_e32 v152, v106, v138
	v_add_f32_e32 v156, v107, v139
	v_mov_b32_e32 v151, v133
	v_cvt_pk_fp8_f32 v151, v152, v156
	v_add_f32_e32 v153, v112, v136
	v_add_f32_e32 v155, v113, v137
	v_cvt_pk_fp8_f32 v150, v153, v155 op_sel:[0,0,1]
	v_add_f32_e32 v152, v108, v140
	v_add_f32_e32 v153, v109, v141
	v_cvt_pk_fp8_f32 v151, v152, v153 op_sel:[0,0,1]
	v_add_f32_e32 v153, v86, v142
	v_add_f32_e32 v155, v87, v143
	v_mov_b32_e32 v152, v133
	v_cvt_pk_fp8_f32 v152, v153, v155
	v_add_f32_e32 v155, v82, v146
	v_mov_b32_e32 v153, v133
	v_cvt_pk_fp8_f32 v153, v155, v158
	v_add_f32_e32 v156, v88, v144
	v_add_f32_e32 v157, v89, v145
	v_cvt_pk_fp8_f32 v152, v156, v157 op_sel:[0,0,1]
	v_add_f32_e32 v155, v84, v148
	v_add_f32_e32 v156, v85, v149
	v_cvt_pk_fp8_f32 v153, v155, v156 op_sel:[0,0,1]
	v_add_f32_e32 v155, v78, v134
	v_add_f32_e32 v135, v79, v135
	v_mov_b32_e32 v134, v133
	v_cvt_pk_fp8_f32 v134, v155, v135
	v_add_f32_e32 v138, v74, v138
	v_add_f32_e32 v139, v75, v139
	v_mov_b32_e32 v135, v133
	v_cvt_pk_fp8_f32 v135, v138, v139
	v_add_f32_e32 v136, v80, v136
	v_add_f32_e32 v137, v81, v137
	v_cvt_pk_fp8_f32 v134, v136, v137 op_sel:[0,0,1]
	v_add_f32_e32 v136, v76, v140
	v_add_f32_e32 v137, v77, v141
	v_cvt_pk_fp8_f32 v135, v136, v137 op_sel:[0,0,1]
	v_add_f32_e32 v137, v70, v142
	v_add_f32_e32 v138, v71, v143
	v_mov_b32_e32 v136, v133
	v_cvt_pk_fp8_f32 v136, v137, v138
	v_add_f32_e32 v138, v66, v146
	v_add_f32_e32 v141, v67, v147
	v_mov_b32_e32 v137, v133
	v_cvt_pk_fp8_f32 v137, v138, v141
	v_add_f32_e32 v139, v72, v144
	v_add_f32_e32 v140, v73, v145
	s_or_b32 s12, s7, 8
	v_cvt_pk_fp8_f32 v136, v139, v140 op_sel:[0,0,1]
	v_add_f32_e32 v138, v68, v148
	v_add_f32_e32 v139, v69, v149
	v_add_u32_e32 v154, s12, v160
	v_cvt_pk_fp8_f32 v137, v138, v139 op_sel:[0,0,1]
	v_mad_i64_i32 v[138:139], s[10:11], v154, s6, v[130:131]
	v_lshl_add_u64 v[138:139], v[138:139], 0, v[132:133]
	global_store_dwordx4 v[138:139], v[150:153], off sc1
	global_store_dwordx4 v[138:139], v[134:137], off offset:1024 sc1
	ds_read_b128 v[134:137], v1 offset:512
	ds_read_b128 v[138:141], v1 offset:576
	ds_read_b128 v[142:145], v1 offset:640
	ds_read_b128 v[146:149], v1 offset:704
	v_add_u32_e32 v1, 2, v160
	v_add_u32_e32 v150, s7, v1
	v_mad_i64_i32 v[154:155], s[10:11], v150, s6, v[130:131]
	s_waitcnt lgkmcnt(3)
	v_add_f32_e32 v151, v62, v134
	v_add_f32_e32 v152, v63, v135
	v_mov_b32_e32 v150, v133
	v_cvt_pk_fp8_f32 v150, v151, v152
	s_waitcnt lgkmcnt(2)
	v_add_f32_e32 v152, v58, v138
	v_add_f32_e32 v157, v59, v139
	v_mov_b32_e32 v151, v133
	v_cvt_pk_fp8_f32 v151, v152, v157
	v_add_f32_e32 v153, v64, v136
	v_add_f32_e32 v156, v65, v137
	v_cvt_pk_fp8_f32 v150, v153, v156 op_sel:[0,0,1]
	v_add_f32_e32 v152, v60, v140
	v_add_f32_e32 v153, v61, v141
	v_cvt_pk_fp8_f32 v151, v152, v153 op_sel:[0,0,1]
	s_waitcnt lgkmcnt(1)
	v_add_f32_e32 v153, v54, v142
	v_add_f32_e32 v156, v55, v143
	v_mov_b32_e32 v152, v133
	v_cvt_pk_fp8_f32 v152, v153, v156
	s_waitcnt lgkmcnt(0)
	v_add_f32_e32 v156, v50, v146
	v_add_f32_e32 v159, v51, v147
	v_mov_b32_e32 v153, v133
	v_cvt_pk_fp8_f32 v153, v156, v159
	v_add_f32_e32 v157, v56, v144
	v_add_f32_e32 v158, v57, v145
	v_cvt_pk_fp8_f32 v152, v157, v158 op_sel:[0,0,1]
	v_add_f32_e32 v156, v52, v148
	v_add_f32_e32 v157, v53, v149
	v_cvt_pk_fp8_f32 v153, v156, v157 op_sel:[0,0,1]
	v_lshl_add_u64 v[162:163], v[154:155], 0, v[132:133]
	v_add_f32_e32 v155, v46, v134
	v_add_f32_e32 v156, v47, v135
	v_mov_b32_e32 v154, v133
	v_cvt_pk_fp8_f32 v154, v155, v156
	v_add_f32_e32 v156, v42, v138
	v_add_f32_e32 v159, v43, v139
	v_mov_b32_e32 v155, v133
	v_cvt_pk_fp8_f32 v155, v156, v159
	v_add_f32_e32 v157, v48, v136
	v_add_f32_e32 v158, v49, v137
	v_cvt_pk_fp8_f32 v154, v157, v158 op_sel:[0,0,1]
	v_add_f32_e32 v156, v44, v140
	v_add_f32_e32 v157, v45, v141
	v_cvt_pk_fp8_f32 v155, v156, v157 op_sel:[0,0,1]
	v_add_f32_e32 v157, v38, v142
	v_add_f32_e32 v158, v39, v143
	v_mov_b32_e32 v156, v133
	v_cvt_pk_fp8_f32 v156, v157, v158
	v_add_f32_e32 v158, v34, v146
	v_add_f32_e32 v161, v35, v147
	v_mov_b32_e32 v157, v133
	v_cvt_pk_fp8_f32 v157, v158, v161
	v_add_f32_e32 v159, v40, v144
	v_add_f32_e32 v160, v41, v145
	v_cvt_pk_fp8_f32 v156, v159, v160 op_sel:[0,0,1]
	v_add_f32_e32 v158, v36, v148
	v_add_f32_e32 v159, v37, v149
	v_add_u32_e32 v1, s12, v1
	v_cvt_pk_fp8_f32 v157, v158, v159 op_sel:[0,0,1]
	v_mad_i64_i32 v[130:131], s[6:7], v1, s6, v[130:131]
	v_add_f32_e32 v1, v30, v134
	v_add_f32_e32 v159, v31, v135
	v_mov_b32_e32 v158, v133
	v_cvt_pk_fp8_f32 v158, v1, v159
	v_add_f32_e32 v1, v26, v138
	v_add_f32_e32 v164, v27, v139
	v_mov_b32_e32 v159, v133
	v_cvt_pk_fp8_f32 v159, v1, v164
	v_add_f32_e32 v160, v32, v136
	v_add_f32_e32 v161, v33, v137
	v_cvt_pk_fp8_f32 v158, v160, v161 op_sel:[0,0,1]
	v_add_f32_e32 v1, v28, v140
	v_add_f32_e32 v160, v29, v141
	v_cvt_pk_fp8_f32 v159, v1, v160 op_sel:[0,0,1]
	v_add_f32_e32 v1, v22, v142
	v_add_f32_e32 v161, v23, v143
	v_mov_b32_e32 v160, v133
	v_cvt_pk_fp8_f32 v160, v1, v161
	v_add_f32_e32 v1, v14, v146
	v_add_f32_e32 v166, v15, v147
	v_mov_b32_e32 v161, v133
	v_cvt_pk_fp8_f32 v161, v1, v166
	v_add_f32_e32 v164, v24, v144
	v_add_f32_e32 v165, v25, v145
	v_cvt_pk_fp8_f32 v160, v164, v165 op_sel:[0,0,1]
	v_add_f32_e32 v1, v16, v148
	v_add_f32_e32 v164, v17, v149
	v_cvt_pk_fp8_f32 v161, v1, v164 op_sel:[0,0,1]
	v_lshl_add_u64 v[164:165], v[130:131], 0, v[132:133]
	v_add_f32_e32 v1, v10, v134
	v_add_f32_e32 v131, v11, v135
	v_mov_b32_e32 v130, v133
	v_cvt_pk_fp8_f32 v130, v1, v131
	v_add_f32_e32 v1, v6, v138
	v_add_f32_e32 v135, v7, v139
	v_mov_b32_e32 v131, v133
	v_cvt_pk_fp8_f32 v131, v1, v135
	v_add_f32_e32 v132, v12, v136
	v_add_f32_e32 v134, v13, v137
	v_cvt_pk_fp8_f32 v130, v132, v134 op_sel:[0,0,1]
	v_add_f32_e32 v1, v8, v140
	v_add_f32_e32 v132, v9, v141
	v_cvt_pk_fp8_f32 v131, v1, v132 op_sel:[0,0,1]
	v_add_f32_e32 v1, v2, v142
	v_add_f32_e32 v134, v3, v143
	v_mov_b32_e32 v132, v133
	v_cvt_pk_fp8_f32 v132, v1, v134
	v_add_f32_e32 v1, v18, v146
	v_add_f32_e32 v134, v19, v147
	v_cvt_pk_fp8_f32 v133, v1, v134
	v_add_f32_e32 v135, v4, v144
	v_add_f32_e32 v136, v5, v145
	v_add_f32_e32 v1, v20, v148
	v_add_f32_e32 v134, v21, v149
	v_cvt_pk_fp8_f32 v132, v135, v136 op_sel:[0,0,1]
	v_cvt_pk_fp8_f32 v133, v1, v134 op_sel:[0,0,1]
	global_store_dwordx4 v[162:163], v[150:153], off sc1
	global_store_dwordx4 v[162:163], v[154:157], off offset:1024 sc1
	global_store_dwordx4 v[164:165], v[158:161], off sc1
	global_store_dwordx4 v[164:165], v[130:133], off offset:1024 sc1

.LBB1_29:
	s_andn2_b64 vcc, exec, s[6:7]
	s_cbranch_vccnz .LBB1_31
	v_mov_b32_e32 v1, v0
	s_movk_i32 s7, 0x60
	v_and_b32_e32 v130, 15, v1
	v_lshrrev_b32_e32 v131, 1, v1
	v_and_or_b32 v130, v131, s7, v130
	v_ashrrev_i32_e32 v131, 2, v1
	v_lshlrev_b32_e32 v132, 1, v1
	v_and_b32_e32 v131, 0xffffffc0, v131
	v_and_b32_e32 v132, 32, v132
	v_add3_u32 v131, 0, v131, v132
	v_lshl_add_u32 v132, v130, 2, 0
	v_add_u32_e32 v135, 0x20000, v132
	ds_read2_b32 v[132:133], v135 offset1:16
	v_lshrrev_b32_e32 v134, 3, v1
	v_and_b32_e32 v134, 4, v134
	v_mul_u32_u24_e32 v130, 0x110, v130
	v_add3_u32 v130, v131, v134, v130
	s_waitcnt lgkmcnt(0)
	v_add_f32_e32 v134, v132, v126
	v_add_f32_e32 v136, v132, v127
	v_mov_b32_e32 v137, 0
	v_cvt_pk_fp8_f32 v137, v134, v136
	v_add_f32_e32 v138, v132, v122
	v_add_f32_e32 v139, v132, v123
	v_mov_b32_e32 v140, 0
	v_cvt_pk_fp8_f32 v140, v138, v139
	v_add_f32_e32 v134, v132, v128
	v_add_f32_e32 v136, v132, v129
	v_cvt_pk_fp8_f32 v137, v134, v136 op_sel:[0,0,1]
	v_add_f32_e32 v134, v132, v124
	v_add_f32_e32 v136, v132, v125
	v_cvt_pk_fp8_f32 v140, v134, v136 op_sel:[0,0,1]
	v_add_f32_e32 v134, v132, v118
	v_add_f32_e32 v136, v132, v119
	v_mov_b32_e32 v138, 0
	v_cvt_pk_fp8_f32 v138, v134, v136
	v_add_f32_e32 v139, v132, v114
	v_add_f32_e32 v141, v132, v115
	v_mov_b32_e32 v142, 0
	v_cvt_pk_fp8_f32 v142, v139, v141
	v_add_f32_e32 v134, v132, v120
	v_add_f32_e32 v136, v132, v121
	v_cvt_pk_fp8_f32 v138, v134, v136 op_sel:[0,0,1]
	v_add_f32_e32 v134, v132, v116
	v_add_f32_e32 v136, v132, v117
	v_cvt_pk_fp8_f32 v142, v134, v136 op_sel:[0,0,1]
	v_add_f32_e32 v134, v132, v62
	v_add_f32_e32 v136, v132, v63
	v_mov_b32_e32 v139, 0
	v_cvt_pk_fp8_f32 v139, v134, v136
	v_add_f32_e32 v141, v132, v58
	v_add_f32_e32 v143, v132, v59
	v_mov_b32_e32 v144, 0
	v_cvt_pk_fp8_f32 v144, v141, v143
	v_add_f32_e32 v134, v132, v64
	v_add_f32_e32 v136, v132, v65
	v_cvt_pk_fp8_f32 v139, v134, v136 op_sel:[0,0,1]
	v_add_f32_e32 v134, v132, v60
	v_add_f32_e32 v136, v132, v61
	v_cvt_pk_fp8_f32 v144, v134, v136 op_sel:[0,0,1]
	v_add_f32_e32 v134, v132, v54
	v_add_f32_e32 v136, v132, v55
	v_mov_b32_e32 v141, 0
	v_cvt_pk_fp8_f32 v141, v134, v136
	v_add_f32_e32 v143, v132, v50
	v_add_f32_e32 v145, v132, v51
	v_mov_b32_e32 v146, 0
	v_cvt_pk_fp8_f32 v146, v143, v145
	v_add_f32_e32 v134, v132, v56
	v_add_f32_e32 v136, v132, v57
	v_cvt_pk_fp8_f32 v141, v134, v136 op_sel:[0,0,1]
	v_add_f32_e32 v134, v132, v52
	v_add_f32_e32 v132, v132, v53
	v_cvt_pk_fp8_f32 v146, v134, v132 op_sel:[0,0,1]
	v_add_f32_e32 v132, v133, v102
	v_add_f32_e32 v134, v133, v103
	v_mov_b32_e32 v136, 0
	ds_write2_b32 v130, v137, v140 offset1:2
	ds_write2_b32 v130, v138, v142 offset0:4 offset1:6
	ds_write2_b32 v130, v139, v144 offset0:32 offset1:34
	ds_write2_b32 v130, v141, v146 offset0:36 offset1:38
	v_cvt_pk_fp8_f32 v136, v132, v134
	v_add_f32_e32 v137, v133, v98
	v_add_f32_e32 v138, v133, v99
	v_mov_b32_e32 v139, 0
	v_cvt_pk_fp8_f32 v139, v137, v138
	v_add_f32_e32 v132, v133, v104
	v_add_f32_e32 v134, v133, v105
	v_cvt_pk_fp8_f32 v136, v132, v134 op_sel:[0,0,1]
	v_add_f32_e32 v132, v133, v100
	v_add_f32_e32 v134, v133, v101
	v_cvt_pk_fp8_f32 v139, v132, v134 op_sel:[0,0,1]
	v_add_f32_e32 v132, v133, v94
	v_add_f32_e32 v137, v133, v95
	v_mov_b32_e32 v138, 0
	v_cvt_pk_fp8_f32 v138, v132, v137
	v_add_f32_e32 v140, v133, v90
	v_add_f32_e32 v141, v133, v91
	v_mov_b32_e32 v142, 0
	v_cvt_pk_fp8_f32 v142, v140, v141
	v_add_f32_e32 v132, v133, v96
	v_add_f32_e32 v137, v133, v97
	v_cvt_pk_fp8_f32 v138, v132, v137 op_sel:[0,0,1]
	v_add_f32_e32 v132, v133, v92
	v_add_f32_e32 v137, v133, v93
	v_cvt_pk_fp8_f32 v142, v132, v137 op_sel:[0,0,1]
	v_add_f32_e32 v132, v133, v46
	v_add_f32_e32 v137, v133, v47
	v_mov_b32_e32 v140, 0
	v_cvt_pk_fp8_f32 v140, v132, v137
	v_add_f32_e32 v141, v133, v42
	v_add_f32_e32 v143, v133, v43
	v_mov_b32_e32 v144, 0
	v_cvt_pk_fp8_f32 v144, v141, v143
	v_add_f32_e32 v132, v133, v48
	v_add_f32_e32 v137, v133, v49
	v_cvt_pk_fp8_f32 v140, v132, v137 op_sel:[0,0,1]
	v_add_f32_e32 v132, v133, v44
	v_add_f32_e32 v137, v133, v45
	v_cvt_pk_fp8_f32 v144, v132, v137 op_sel:[0,0,1]
	v_add_f32_e32 v132, v133, v38
	v_add_f32_e32 v137, v133, v39
	v_mov_b32_e32 v141, 0
	v_cvt_pk_fp8_f32 v141, v132, v137
	v_add_f32_e32 v143, v133, v34
	v_add_f32_e32 v145, v133, v35
	v_mov_b32_e32 v146, 0
	v_cvt_pk_fp8_f32 v146, v143, v145
	v_add_f32_e32 v132, v133, v40
	v_add_f32_e32 v137, v133, v41
	v_cvt_pk_fp8_f32 v141, v132, v137 op_sel:[0,0,1]
	v_add_f32_e32 v132, v133, v36
	v_add_f32_e32 v133, v133, v37
	v_cvt_pk_fp8_f32 v146, v132, v133 op_sel:[0,0,1]
	ds_read2_b32 v[132:133], v135 offset0:128 offset1:144
	v_add_u32_e32 v134, 0x1000, v130
	ds_write2_b32 v134, v136, v139 offset0:64 offset1:66
	ds_write2_b32 v134, v138, v142 offset0:68 offset1:70
	ds_write2_b32 v134, v140, v144 offset0:96 offset1:98
	ds_write2_b32 v134, v141, v146 offset0:100 offset1:102
	v_mov_b32_e32 v136, 0
	v_mov_b32_e32 v139, 0
	s_waitcnt lgkmcnt(4)
	v_add_f32_e32 v134, v132, v110
	v_add_f32_e32 v135, v132, v111
	v_cvt_pk_fp8_f32 v136, v134, v135
	v_add_f32_e32 v137, v132, v106
	v_add_f32_e32 v138, v132, v107
	v_cvt_pk_fp8_f32 v139, v137, v138
	v_add_f32_e32 v134, v132, v112
	v_add_f32_e32 v135, v132, v113
	v_cvt_pk_fp8_f32 v136, v134, v135 op_sel:[0,0,1]
	v_add_f32_e32 v134, v132, v108
	v_add_f32_e32 v135, v132, v109
	v_cvt_pk_fp8_f32 v139, v134, v135 op_sel:[0,0,1]
	v_add_f32_e32 v135, v132, v86
	v_add_f32_e32 v137, v132, v87
	v_mov_b32_e32 v138, 0
	v_cvt_pk_fp8_f32 v138, v135, v137
	v_add_f32_e32 v140, v132, v82
	v_add_f32_e32 v141, v132, v83
	v_mov_b32_e32 v142, 0
	v_cvt_pk_fp8_f32 v142, v140, v141
	v_add_f32_e32 v135, v132, v88
	v_add_f32_e32 v137, v132, v89
	v_cvt_pk_fp8_f32 v138, v135, v137 op_sel:[0,0,1]
	v_add_f32_e32 v135, v132, v84
	v_add_f32_e32 v137, v132, v85
	v_cvt_pk_fp8_f32 v142, v135, v137 op_sel:[0,0,1]
	v_add_f32_e32 v135, v132, v30
	v_add_f32_e32 v137, v132, v31
	v_mov_b32_e32 v140, 0
	v_cvt_pk_fp8_f32 v140, v135, v137
	v_add_f32_e32 v141, v132, v26
	v_add_f32_e32 v143, v132, v27
	v_mov_b32_e32 v144, 0
	v_cvt_pk_fp8_f32 v144, v141, v143
	v_add_f32_e32 v135, v132, v32
	v_add_f32_e32 v137, v132, v33
	v_cvt_pk_fp8_f32 v140, v135, v137 op_sel:[0,0,1]
	v_add_f32_e32 v135, v132, v28
	v_add_f32_e32 v137, v132, v29
	v_cvt_pk_fp8_f32 v144, v135, v137 op_sel:[0,0,1]
	v_add_f32_e32 v135, v132, v22
	v_add_f32_e32 v137, v132, v23
	v_mov_b32_e32 v141, 0
	v_cvt_pk_fp8_f32 v141, v135, v137
	v_add_f32_e32 v143, v132, v14
	v_add_f32_e32 v145, v132, v15
	v_mov_b32_e32 v146, 0
	v_cvt_pk_fp8_f32 v146, v143, v145
	v_add_f32_e32 v135, v132, v24
	v_add_f32_e32 v137, v132, v25
	v_cvt_pk_fp8_f32 v141, v135, v137 op_sel:[0,0,1]
	v_add_f32_e32 v135, v132, v16
	v_add_f32_e32 v132, v132, v17
	v_add_u32_e32 v134, 0x8800, v130
	v_cvt_pk_fp8_f32 v146, v135, v132 op_sel:[0,0,1]
	ds_write2_b32 v134, v136, v139 offset1:2
	ds_write2_b32 v134, v138, v142 offset0:4 offset1:6
	ds_write2_b32 v134, v140, v144 offset0:32 offset1:34
	ds_write2_b32 v134, v141, v146 offset0:36 offset1:38
	v_add_f32_e32 v132, v133, v78
	v_add_f32_e32 v134, v133, v79
	v_mov_b32_e32 v135, 0
	v_cvt_pk_fp8_f32 v135, v132, v134
	v_add_f32_e32 v136, v133, v74
	v_add_f32_e32 v137, v133, v75
	v_mov_b32_e32 v138, 0
	v_cvt_pk_fp8_f32 v138, v136, v137
	v_add_f32_e32 v132, v133, v80
	v_add_f32_e32 v134, v133, v81
	v_cvt_pk_fp8_f32 v135, v132, v134 op_sel:[0,0,1]
	v_add_f32_e32 v132, v133, v76
	v_add_f32_e32 v134, v133, v77
	v_cvt_pk_fp8_f32 v138, v132, v134 op_sel:[0,0,1]
	v_add_f32_e32 v132, v133, v70
	v_add_f32_e32 v134, v133, v71
	v_mov_b32_e32 v136, 0
	v_cvt_pk_fp8_f32 v136, v132, v134
	v_add_f32_e32 v137, v133, v66
	v_add_f32_e32 v139, v133, v67
	v_mov_b32_e32 v140, 0
	v_cvt_pk_fp8_f32 v140, v137, v139
	v_add_f32_e32 v132, v133, v72
	v_add_f32_e32 v134, v133, v73
	v_cvt_pk_fp8_f32 v136, v132, v134 op_sel:[0,0,1]
	v_add_f32_e32 v132, v133, v68
	v_add_f32_e32 v134, v133, v69
	v_cvt_pk_fp8_f32 v140, v132, v134 op_sel:[0,0,1]
	v_add_f32_e32 v132, v133, v10
	v_add_f32_e32 v134, v133, v11
	v_mov_b32_e32 v137, 0
	v_cvt_pk_fp8_f32 v137, v132, v134
	v_add_f32_e32 v139, v133, v6
	v_add_f32_e32 v141, v133, v7
	v_mov_b32_e32 v142, 0
	v_cvt_pk_fp8_f32 v142, v139, v141
	v_add_f32_e32 v132, v133, v12
	v_add_f32_e32 v134, v133, v13
	v_cvt_pk_fp8_f32 v137, v132, v134 op_sel:[0,0,1]
	v_add_f32_e32 v132, v133, v8
	v_add_f32_e32 v134, v133, v9
	v_cvt_pk_fp8_f32 v142, v132, v134 op_sel:[0,0,1]
	v_add_f32_e32 v132, v133, v2
	v_add_f32_e32 v134, v133, v3
	v_mov_b32_e32 v139, 0
	v_cvt_pk_fp8_f32 v139, v132, v134
	v_add_f32_e32 v141, v133, v18
	v_add_f32_e32 v143, v133, v19
	v_mov_b32_e32 v144, 0
	v_cvt_pk_fp8_f32 v144, v141, v143
	v_add_f32_e32 v132, v133, v4
	v_add_f32_e32 v134, v133, v5
	s_lshl_b32 s11, s3, 2
	s_and_b32 s6, s3, 0x1f8
	v_cvt_pk_fp8_f32 v139, v132, v134 op_sel:[0,0,1]
	v_add_f32_e32 v132, v133, v20
	v_add_f32_e32 v133, v133, v21
	s_and_b32 s11, s11, 4
	v_add_u32_e32 v130, 0x9800, v130
	v_cvt_pk_fp8_f32 v144, v132, v133 op_sel:[0,0,1]
	s_or_b32 s6, s6, s11
	ds_write2_b32 v130, v135, v138 offset0:64 offset1:66
	ds_write2_b32 v130, v136, v140 offset0:68 offset1:70
	ds_write2_b32 v130, v137, v142 offset0:96 offset1:98
	ds_write2_b32 v130, v139, v144 offset0:100 offset1:102
	v_lshlrev_b32_e32 v130, 4, v1
	s_add_i32 s11, s6, 0xffffff00
	v_ashrrev_i32_e32 v136, 10, v1
	v_and_b32_e32 v130, 0xf0, v130
	v_add_u32_e32 v136, s11, v136
	s_movk_i32 s10, 0x110
	v_add_u32_e32 v140, 0, v130
	v_ashrrev_i32_e32 v138, 4, v1
	v_ashrrev_i32_e32 v137, 31, v136
	v_mad_u64_u32 v[132:133], s[12:13], v138, s10, v[140:141]
	v_lshlrev_b64 v[136:137], 6, v[136:137]
	s_waitcnt lgkmcnt(0)
	s_barrier
	ds_read_b128 v[132:135], v132
	v_and_or_b32 v136, v138, 63, v136
	s_movk_i32 s12, 0x480
	v_mov_b64_e32 v[142:143], s[0:1]
	s_lshl_b32 s6, s3, 7
	v_mad_u64_u32 v[138:139], s[0:1], v136, s12, v[142:143]
	s_mov_b32 s7, 0
	s_and_b32 s6, s6, 0x300
	v_mad_i32_i24 v139, v137, s12, v139
	v_add_u32_e32 v141, 0x200, v1
	v_mov_b32_e32 v131, 0
	v_lshl_add_u64 v[136:137], v[138:139], 0, s[6:7]
	v_ashrrev_i32_e32 v146, 4, v141
	v_lshl_add_u64 v[144:145], v[136:137], 0, v[130:131]
	v_mad_u64_u32 v[136:137], s[0:1], v146, s10, v[140:141]
	ds_read_b128 v[136:139], v136
	s_waitcnt lgkmcnt(1)
	global_store_dwordx4 v[144:145], v[132:135], off offset:128 sc1
	s_nop 1
	v_ashrrev_i32_e32 v132, 10, v141
	v_add_u32_e32 v132, s11, v132
	v_ashrrev_i32_e32 v133, 31, v132
	v_lshlrev_b64 v[132:133], 6, v[132:133]
	v_and_or_b32 v132, v146, 63, v132
	v_mad_u64_u32 v[134:135], s[0:1], v132, s12, v[142:143]
	v_mad_i32_i24 v135, v133, s12, v135
	v_lshl_add_u64 v[132:133], v[134:135], 0, s[6:7]
	v_lshl_add_u64 v[132:133], v[132:133], 0, v[130:131]
	s_waitcnt lgkmcnt(0)
	global_store_dwordx4 v[132:133], v[136:139], off offset:128 sc1
	s_nop 1
	v_add_u32_e32 v136, 0x400, v1
	v_ashrrev_i32_e32 v138, 4, v136
	v_ashrrev_i32_e32 v136, 10, v136
	v_add_u32_e32 v136, s11, v136
	v_ashrrev_i32_e32 v137, 31, v136
	v_mad_u64_u32 v[132:133], s[0:1], v138, s10, v[140:141]
	v_lshlrev_b64 v[136:137], 6, v[136:137]
	ds_read_b128 v[132:135], v132
	v_and_or_b32 v136, v138, 63, v136
	v_mad_u64_u32 v[138:139], s[0:1], v136, s12, v[142:143]
	v_mad_i32_i24 v139, v137, s12, v139
	v_add_u32_e32 v141, 0x600, v1
	v_lshl_add_u64 v[136:137], v[138:139], 0, s[6:7]
	v_ashrrev_i32_e32 v146, 4, v141
	v_lshl_add_u64 v[144:145], v[136:137], 0, v[130:131]
	v_mad_u64_u32 v[136:137], s[0:1], v146, s10, v[140:141]
	ds_read_b128 v[136:139], v136
	s_waitcnt lgkmcnt(1)
	global_store_dwordx4 v[144:145], v[132:135], off offset:128 sc1
	s_nop 1
	v_ashrrev_i32_e32 v132, 10, v141
	v_add_u32_e32 v132, s11, v132
	v_ashrrev_i32_e32 v133, 31, v132
	v_lshlrev_b64 v[132:133], 6, v[132:133]
	v_and_or_b32 v132, v146, 63, v132
	v_mad_u64_u32 v[134:135], s[0:1], v132, s12, v[142:143]
	v_mad_i32_i24 v135, v133, s12, v135
	v_lshl_add_u64 v[132:133], v[134:135], 0, s[6:7]
	v_lshl_add_u64 v[132:133], v[132:133], 0, v[130:131]
	s_waitcnt lgkmcnt(0)
	global_store_dwordx4 v[132:133], v[136:139], off offset:128 sc1
	s_nop 1
	v_add_u32_e32 v136, 0x800, v1
	v_ashrrev_i32_e32 v138, 4, v136
	v_ashrrev_i32_e32 v136, 10, v136
	v_add_u32_e32 v136, s11, v136
	v_ashrrev_i32_e32 v137, 31, v136
	v_mad_u64_u32 v[132:133], s[0:1], v138, s10, v[140:141]
	v_lshlrev_b64 v[136:137], 6, v[136:137]
	ds_read_b128 v[132:135], v132
	v_and_or_b32 v136, v138, 63, v136
	v_mad_u64_u32 v[138:139], s[0:1], v136, s12, v[142:143]
	v_mad_i32_i24 v139, v137, s12, v139
	v_add_u32_e32 v141, 0xa00, v1
	v_lshl_add_u64 v[136:137], v[138:139], 0, s[6:7]
	v_ashrrev_i32_e32 v146, 4, v141
	v_lshl_add_u64 v[144:145], v[136:137], 0, v[130:131]
	v_mad_u64_u32 v[136:137], s[0:1], v146, s10, v[140:141]
	ds_read_b128 v[136:139], v136
	s_waitcnt lgkmcnt(1)
	global_store_dwordx4 v[144:145], v[132:135], off offset:128 sc1
	s_nop 1
	v_ashrrev_i32_e32 v132, 10, v141
	v_add_u32_e32 v132, s11, v132
	v_ashrrev_i32_e32 v133, 31, v132
	v_lshlrev_b64 v[132:133], 6, v[132:133]
	v_and_or_b32 v132, v146, 63, v132
	v_mad_u64_u32 v[134:135], s[0:1], v132, s12, v[142:143]
	v_mad_i32_i24 v135, v133, s12, v135
	v_lshl_add_u64 v[132:133], v[134:135], 0, s[6:7]
	v_lshl_add_u64 v[132:133], v[132:133], 0, v[130:131]
	s_waitcnt lgkmcnt(0)
	global_store_dwordx4 v[132:133], v[136:139], off offset:128 sc1
	s_nop 1
	v_add_u32_e32 v136, 0xc00, v1
	v_ashrrev_i32_e32 v138, 4, v136
	v_ashrrev_i32_e32 v136, 10, v136
	v_add_u32_e32 v136, s11, v136
	v_ashrrev_i32_e32 v137, 31, v136
	v_mad_u64_u32 v[132:133], s[0:1], v138, s10, v[140:141]
	v_lshlrev_b64 v[136:137], 6, v[136:137]
	ds_read_b128 v[132:135], v132
	v_and_or_b32 v136, v138, 63, v136
	v_mad_u64_u32 v[138:139], s[0:1], v136, s12, v[142:143]
	v_mad_i32_i24 v139, v137, s12, v139
	v_add_u32_e32 v1, 0xe00, v1
	v_lshl_add_u64 v[136:137], v[138:139], 0, s[6:7]
	v_ashrrev_i32_e32 v141, 4, v1
	v_lshl_add_u64 v[144:145], v[136:137], 0, v[130:131]
	v_mad_u64_u32 v[136:137], s[0:1], v141, s10, v[140:141]
	v_ashrrev_i32_e32 v1, 10, v1
	ds_read_b128 v[136:139], v136
	s_waitcnt lgkmcnt(1)
	global_store_dwordx4 v[144:145], v[132:135], off offset:128 sc1
	s_nop 1
	v_add_u32_e32 v132, s11, v1
	v_ashrrev_i32_e32 v133, 31, v132
	v_lshlrev_b64 v[132:133], 6, v[132:133]
	v_and_or_b32 v1, v141, 63, v132
	v_mad_u64_u32 v[134:135], s[0:1], v1, s12, v[142:143]
	v_mad_i32_i24 v135, v133, s12, v135
	v_lshl_add_u64 v[132:133], v[134:135], 0, s[6:7]
	v_lshl_add_u64 v[130:131], v[132:133], 0, v[130:131]
	s_waitcnt lgkmcnt(0)
	global_store_dwordx4 v[130:131], v[136:139], off offset:128 sc1

.LBB1_32:
	s_bfe_u32 s6, s2, 0x20003
	s_movk_i32 s2, 0xff
	s_lshl_b32 s12, s6, 8
	v_cmp_lt_u32_e32 vcc, s2, v0
	s_ashr_i32 s2, s3, 1
	s_lshr_b32 s3, s3, 1
	s_and_b32 s2, s2, -8
	s_and_b32 s3, s3, 6
	s_or_b32 s2, s2, s3
	s_bitset1_b32 s12, 7
	s_lshl_b32 s3, s6, 14
	s_add_u32 s3, s8, s3
	s_addc_u32 s6, s9, 0
	s_movk_i32 s0, 0x100
	s_add_u32 s10, s3, 0x1500000
	v_cmp_gt_u32_e64 s[0:1], s0, v0
	s_addc_u32 s11, s6, 0
	s_ashr_i32 s3, s2, 31
	s_and_saveexec_b64 s[6:7], vcc
	s_xor_b64 s[6:7], exec, s[6:7]
	s_mul_i32 s8, s2, 0x480
	s_mul_hi_i32 s9, s2, 0x480
	s_add_u32 s8, s8, s12
	s_addc_u32 s9, s9, 0
	s_lshl_b64 s[8:9], s[8:9], 6
	s_add_u32 s8, s4, s8
	s_addc_u32 s9, s5, s9
	s_or_saveexec_b64 s[6:7], s[6:7]
	v_mov_b64_e32 v[136:137], s[8:9]
	s_xor_b64 exec, exec, s[6:7]
	s_lshl_b64 s[8:9], s[2:3], 16
	s_add_u32 s8, s10, s8
	s_addc_u32 s9, s11, s9
	v_mov_b64_e32 v[136:137], s[8:9]
	s_or_b64 exec, exec, s[6:7]
	v_mov_b32_e32 v130, 0x3fb8aa3b
	v_and_b32_e32 v134, 48, v0
	v_cndmask_b32_e64 v138, 1.0, v130, s[0:1]
	s_add_i32 s0, 0, 0x20000
	v_and_b32_e32 v130, 0xffffff00, v0
	v_add_u32_e32 v131, s0, v134
	v_add_u32_e32 v139, v131, v130
	ds_read_b128 v[140:143], v139
	ds_read_b128 v[144:147], v139 offset:64
	ds_read_b128 v[148:151], v139 offset:128
	ds_read_b128 v[130:133], v139 offset:192
	v_and_b32_e32 v1, 15, v0
	v_lshrrev_b32_e32 v0, 1, v0
	s_movk_i32 s0, 0x60
	v_mov_b32_e32 v135, 0
	v_and_or_b32 v0, v0, s0, v1
	s_waitcnt lgkmcnt(3)
	v_add_f32_e32 v1, v126, v140
	v_add_f32_e32 v126, v127, v141
	v_mul_f32_e32 v1, v138, v1
	v_mul_f32_e32 v127, v138, v126
	v_mov_b32_e32 v126, v135
	v_cvt_pk_fp8_f32 v126, v1, v127
	v_add_f32_e32 v128, v128, v142
	v_add_f32_e32 v127, v129, v143
	v_mul_f32_e32 v1, v138, v128
	v_mul_f32_e32 v127, v138, v127
	v_cvt_pk_fp8_f32 v126, v1, v127 op_sel:[0,0,1]
	s_waitcnt lgkmcnt(2)
	v_add_f32_e32 v1, v122, v144
	v_add_f32_e32 v122, v123, v145
	v_mul_f32_e32 v1, v138, v1
	v_mul_f32_e32 v122, v138, v122
	v_mov_b32_e32 v127, v135
	v_cvt_pk_fp8_f32 v127, v1, v122
	v_add_f32_e32 v123, v124, v146
	v_add_f32_e32 v122, v125, v147
	v_mul_f32_e32 v1, v138, v123
	v_mul_f32_e32 v122, v138, v122
	v_cvt_pk_fp8_f32 v127, v1, v122 op_sel:[0,0,1]
	s_waitcnt lgkmcnt(1)
	v_add_f32_e32 v1, v118, v148
	v_add_f32_e32 v118, v119, v149
	v_mul_f32_e32 v1, v138, v1
	v_mul_f32_e32 v118, v138, v118
	v_mov_b32_e32 v128, v135
	v_cvt_pk_fp8_f32 v128, v1, v118
	v_add_f32_e32 v119, v120, v150
	v_add_f32_e32 v118, v121, v151
	v_mul_f32_e32 v1, v138, v119
	v_mul_f32_e32 v118, v138, v118
	v_cvt_pk_fp8_f32 v128, v1, v118 op_sel:[0,0,1]
	s_waitcnt lgkmcnt(0)
	v_add_f32_e32 v1, v114, v130
	v_add_f32_e32 v114, v115, v131
	v_mul_f32_e32 v1, v138, v1
	v_mul_f32_e32 v114, v138, v114
	v_mov_b32_e32 v129, v135
	v_cvt_pk_fp8_f32 v129, v1, v114
	v_add_f32_e32 v115, v116, v132
	v_add_f32_e32 v114, v117, v133
	v_mul_f32_e32 v1, v138, v115
	v_mul_f32_e32 v114, v138, v114
	v_cvt_pk_fp8_f32 v129, v1, v114 op_sel:[0,0,1]
	v_add_f32_e32 v1, v102, v140
	v_add_f32_e32 v102, v103, v141
	v_mul_f32_e32 v1, v138, v1
	v_mul_f32_e32 v103, v138, v102
	v_mov_b32_e32 v102, v135
	v_cvt_pk_fp8_f32 v102, v1, v103
	v_add_f32_e32 v104, v104, v142
	v_add_f32_e32 v103, v105, v143
	v_mul_f32_e32 v1, v138, v104
	v_mul_f32_e32 v103, v138, v103
	v_cvt_pk_fp8_f32 v102, v1, v103 op_sel:[0,0,1]
	v_add_f32_e32 v1, v98, v144
	v_add_f32_e32 v98, v99, v145
	v_mul_f32_e32 v1, v138, v1
	v_mul_f32_e32 v98, v138, v98
	v_mov_b32_e32 v103, v135
	v_cvt_pk_fp8_f32 v103, v1, v98
	v_add_f32_e32 v99, v100, v146
	v_add_f32_e32 v98, v101, v147
	v_mul_f32_e32 v1, v138, v99
	v_mul_f32_e32 v98, v138, v98
	v_cvt_pk_fp8_f32 v103, v1, v98 op_sel:[0,0,1]
	v_add_f32_e32 v1, v94, v148
	v_add_f32_e32 v94, v95, v149
	v_mul_f32_e32 v1, v138, v1
	v_mul_f32_e32 v94, v138, v94
	v_mov_b32_e32 v104, v135
	v_cvt_pk_fp8_f32 v104, v1, v94
	v_add_f32_e32 v95, v96, v150
	v_add_f32_e32 v94, v97, v151
	v_mul_f32_e32 v1, v138, v95
	v_mul_f32_e32 v94, v138, v94
	v_cvt_pk_fp8_f32 v104, v1, v94 op_sel:[0,0,1]
	v_add_f32_e32 v1, v90, v130
	v_add_f32_e32 v90, v91, v131
	v_mul_f32_e32 v1, v138, v1
	v_mul_f32_e32 v90, v138, v90
	v_mov_b32_e32 v105, v135
	v_cvt_pk_fp8_f32 v105, v1, v90
	v_add_f32_e32 v91, v92, v132
	v_add_f32_e32 v90, v93, v133
	v_mul_f32_e32 v1, v138, v91
	v_mul_f32_e32 v90, v138, v90
	v_cvt_pk_fp8_f32 v105, v1, v90 op_sel:[0,0,1]
	v_lshl_add_u64 v[136:137], v[136:137], 0, v[134:135]
	v_lshlrev_b32_e32 v0, 6, v0
	v_mov_b32_e32 v1, v135
	v_lshl_add_u64 v[90:91], v[136:137], 0, v[0:1]
	global_store_dwordx4 v[90:91], v[126:129], off sc1
	global_store_dwordx4 v[90:91], v[102:105], off offset:1024 sc1
	v_add_f32_e32 v90, v110, v140
	v_mul_f32_e32 v91, v138, v90
	v_add_f32_e32 v90, v111, v141
	v_mul_f32_e32 v92, v138, v90
	v_mov_b32_e32 v90, v135
	v_cvt_pk_fp8_f32 v90, v91, v92
	v_add_f32_e32 v93, v112, v142
	v_add_f32_e32 v92, v113, v143
	v_mul_f32_e32 v91, v138, v93
	v_mul_f32_e32 v92, v138, v92
	v_cvt_pk_fp8_f32 v90, v91, v92 op_sel:[0,0,1]
	v_add_f32_e32 v91, v106, v144
	v_mul_f32_e32 v92, v138, v91
	v_add_f32_e32 v91, v107, v145
	v_mul_f32_e32 v93, v138, v91
	v_mov_b32_e32 v91, v135
	v_cvt_pk_fp8_f32 v91, v92, v93
	v_add_f32_e32 v94, v108, v146
	v_add_f32_e32 v93, v109, v147
	v_mul_f32_e32 v92, v138, v94
	v_mul_f32_e32 v93, v138, v93
	v_add_f32_e32 v86, v86, v148
	v_add_f32_e32 v87, v87, v149
	v_add_f32_e32 v82, v82, v130
	v_add_f32_e32 v83, v83, v131
	v_cvt_pk_fp8_f32 v91, v92, v93 op_sel:[0,0,1]
	v_mul_f32_e32 v86, v138, v86
	v_mul_f32_e32 v87, v138, v87
	v_mov_b32_e32 v92, v135
	v_mul_f32_e32 v82, v138, v82
	v_mul_f32_e32 v83, v138, v83
	v_mov_b32_e32 v93, v135
	v_cvt_pk_fp8_f32 v92, v86, v87
	v_cvt_pk_fp8_f32 v93, v82, v83
	v_add_f32_e32 v88, v88, v150
	v_add_f32_e32 v87, v89, v151
	v_add_f32_e32 v84, v84, v132
	v_add_f32_e32 v83, v85, v133
	v_mul_f32_e32 v86, v138, v88
	v_mul_f32_e32 v87, v138, v87
	v_mul_f32_e32 v82, v138, v84
	v_mul_f32_e32 v83, v138, v83
	v_cvt_pk_fp8_f32 v92, v86, v87 op_sel:[0,0,1]
	v_cvt_pk_fp8_f32 v93, v82, v83 op_sel:[0,0,1]
	v_or_b32_e32 v82, 0x2000, v0
	v_mov_b32_e32 v83, v135
	v_lshl_add_u64 v[84:85], v[136:137], 0, v[82:83]
	v_add_f32_e32 v78, v78, v140
	global_store_dwordx4 v[84:85], v[90:93], off sc1
	v_mul_f32_e32 v84, v138, v78
	v_add_f32_e32 v78, v79, v141
	v_mul_f32_e32 v79, v138, v78
	v_mov_b32_e32 v78, v135
	v_cvt_pk_fp8_f32 v78, v84, v79
	v_add_f32_e32 v80, v80, v142
	v_mul_f32_e32 v79, v138, v80
	v_add_f32_e32 v80, v81, v143
	v_mul_f32_e32 v80, v138, v80
	v_add_f32_e32 v74, v74, v144
	v_add_f32_e32 v75, v75, v145
	v_add_f32_e32 v70, v70, v148
	v_add_f32_e32 v71, v71, v149
	v_add_f32_e32 v66, v66, v130
	v_add_f32_e32 v67, v67, v131
	v_cvt_pk_fp8_f32 v78, v79, v80 op_sel:[0,0,1]
	v_mul_f32_e32 v74, v138, v74
	v_mul_f32_e32 v75, v138, v75
	v_mov_b32_e32 v79, v135
	v_mul_f32_e32 v70, v138, v70
	v_mul_f32_e32 v71, v138, v71
	v_mov_b32_e32 v80, v135
	v_mul_f32_e32 v66, v138, v66
	v_mul_f32_e32 v67, v138, v67
	v_mov_b32_e32 v81, v135
	v_cvt_pk_fp8_f32 v79, v74, v75
	v_cvt_pk_fp8_f32 v80, v70, v71
	v_cvt_pk_fp8_f32 v81, v66, v67
	v_add_f32_e32 v76, v76, v146
	v_add_f32_e32 v75, v77, v147
	v_add_f32_e32 v72, v72, v150
	v_add_f32_e32 v71, v73, v151
	v_add_f32_e32 v68, v68, v132
	v_add_f32_e32 v67, v69, v133
	v_mul_f32_e32 v74, v138, v76
	v_mul_f32_e32 v75, v138, v75
	v_mul_f32_e32 v70, v138, v72
	v_mul_f32_e32 v71, v138, v71
	v_mul_f32_e32 v66, v138, v68
	v_mul_f32_e32 v67, v138, v67
	v_cvt_pk_fp8_f32 v79, v74, v75 op_sel:[0,0,1]
	v_cvt_pk_fp8_f32 v80, v70, v71 op_sel:[0,0,1]
	v_cvt_pk_fp8_f32 v81, v66, v67 op_sel:[0,0,1]
	v_or_b32_e32 v70, 0x2400, v0
	v_mov_b32_e32 v71, v135
	s_or_b32 s0, s2, 1
	v_lshl_add_u64 v[66:67], v[136:137], 0, v[70:71]
	s_ashr_i32 s1, s0, 31
	global_store_dwordx4 v[66:67], v[78:81], off sc1
	s_and_saveexec_b64 s[2:3], vcc
	s_xor_b64 s[2:3], exec, s[2:3]
	s_mul_i32 s6, s0, 0x480
	s_mul_hi_i32 s7, s0, 0x480
	s_add_u32 s6, s6, s12
	s_addc_u32 s7, s7, 0
	s_lshl_b64 s[6:7], s[6:7], 6
	s_add_u32 s6, s4, s6
	s_addc_u32 s7, s5, s7
	s_or_saveexec_b64 s[2:3], s[2:3]
	v_mov_b64_e32 v[72:73], s[6:7]
	s_xor_b64 exec, exec, s[2:3]
	s_lshl_b64 s[0:1], s[0:1], 16
	s_add_u32 s0, s10, s0
	s_addc_u32 s1, s11, s1
	v_mov_b64_e32 v[72:73], s[0:1]
	s_or_b64 exec, exec, s[2:3]
	ds_read_b128 v[74:77], v139 offset:512
	ds_read_b128 v[78:81], v139 offset:576
	ds_read_b128 v[84:87], v139 offset:640
	ds_read_b128 v[66:69], v139 offset:704
	v_lshl_add_u64 v[72:73], v[72:73], 0, v[134:135]
	s_waitcnt lgkmcnt(3)
	v_add_f32_e32 v62, v62, v74
	v_mul_f32_e32 v88, v138, v62
	v_add_f32_e32 v62, v63, v75
	v_mul_f32_e32 v63, v138, v62
	v_add_f32_e32 v64, v64, v76
	v_mov_b32_e32 v62, 0
	s_waitcnt lgkmcnt(0)
	v_add_f32_e32 v50, v50, v66
	v_add_f32_e32 v51, v51, v67
	v_cvt_pk_fp8_f32 v62, v88, v63
	v_mul_f32_e32 v63, v138, v64
	v_add_f32_e32 v64, v65, v77
	v_mul_f32_e32 v50, v138, v50
	v_mul_f32_e32 v51, v138, v51
	v_mov_b32_e32 v65, 0
	v_cvt_pk_fp8_f32 v65, v50, v51
	v_add_f32_e32 v52, v52, v68
	v_add_f32_e32 v51, v53, v69
	v_mul_f32_e32 v50, v138, v52
	v_mul_f32_e32 v51, v138, v51
	v_add_f32_e32 v46, v46, v74
	v_cvt_pk_fp8_f32 v65, v50, v51 op_sel:[0,0,1]
	v_mul_f32_e32 v50, v138, v46
	v_add_f32_e32 v46, v47, v75
	v_mul_f32_e32 v47, v138, v46
	v_mov_b32_e32 v46, 0
	v_cvt_pk_fp8_f32 v46, v50, v47
	v_add_f32_e32 v48, v48, v76
	v_mul_f32_e32 v64, v138, v64
	v_add_f32_e32 v58, v58, v78
	v_add_f32_e32 v59, v59, v79
	v_add_f32_e32 v54, v54, v84
	v_add_f32_e32 v55, v55, v85
	v_mul_f32_e32 v47, v138, v48
	v_add_f32_e32 v48, v49, v77
	v_cvt_pk_fp8_f32 v62, v63, v64 op_sel:[0,0,1]
	v_mul_f32_e32 v58, v138, v58
	v_mul_f32_e32 v59, v138, v59
	v_mov_b32_e32 v63, 0
	v_mul_f32_e32 v54, v138, v54
	v_mul_f32_e32 v55, v138, v55
	v_mov_b32_e32 v64, 0
	v_mul_f32_e32 v48, v138, v48
	v_add_f32_e32 v42, v42, v78
	v_add_f32_e32 v43, v43, v79
	v_add_f32_e32 v38, v38, v84
	v_add_f32_e32 v39, v39, v85
	v_add_f32_e32 v34, v34, v66
	v_add_f32_e32 v35, v35, v67
	v_cvt_pk_fp8_f32 v63, v58, v59
	v_cvt_pk_fp8_f32 v64, v54, v55
	v_cvt_pk_fp8_f32 v46, v47, v48 op_sel:[0,0,1]
	v_mul_f32_e32 v42, v138, v42
	v_mul_f32_e32 v43, v138, v43
	v_mov_b32_e32 v47, 0
	v_mul_f32_e32 v38, v138, v38
	v_mul_f32_e32 v39, v138, v39
	v_mov_b32_e32 v48, 0
	v_mul_f32_e32 v34, v138, v34
	v_mul_f32_e32 v35, v138, v35
	v_mov_b32_e32 v49, 0
	v_cvt_pk_fp8_f32 v47, v42, v43
	v_cvt_pk_fp8_f32 v48, v38, v39
	v_cvt_pk_fp8_f32 v49, v34, v35
	v_add_f32_e32 v60, v60, v80
	v_add_f32_e32 v59, v61, v81
	v_add_f32_e32 v56, v56, v86
	v_add_f32_e32 v55, v57, v87
	v_mul_f32_e32 v58, v138, v60
	v_mul_f32_e32 v59, v138, v59
	v_mul_f32_e32 v54, v138, v56
	v_mul_f32_e32 v55, v138, v55
	v_add_f32_e32 v44, v44, v80
	v_add_f32_e32 v43, v45, v81
	v_add_f32_e32 v40, v40, v86
	v_add_f32_e32 v39, v41, v87
	v_add_f32_e32 v36, v36, v68
	v_add_f32_e32 v35, v37, v69
	v_cvt_pk_fp8_f32 v63, v58, v59 op_sel:[0,0,1]
	v_cvt_pk_fp8_f32 v64, v54, v55 op_sel:[0,0,1]
	v_mul_f32_e32 v42, v138, v44
	v_mul_f32_e32 v43, v138, v43
	v_mul_f32_e32 v38, v138, v40
	v_mul_f32_e32 v39, v138, v39
	v_mul_f32_e32 v34, v138, v36
	v_mul_f32_e32 v35, v138, v35
	v_cvt_pk_fp8_f32 v47, v42, v43 op_sel:[0,0,1]
	v_cvt_pk_fp8_f32 v48, v38, v39 op_sel:[0,0,1]
	v_cvt_pk_fp8_f32 v49, v34, v35 op_sel:[0,0,1]
	v_lshl_add_u64 v[0:1], v[72:73], 0, v[0:1]
	global_store_dwordx4 v[0:1], v[62:65], off sc1
	global_store_dwordx4 v[0:1], v[46:49], off offset:1024 sc1
	v_add_f32_e32 v0, v30, v74
	v_add_f32_e32 v1, v31, v75
	v_mul_f32_e32 v0, v138, v0
	v_mul_f32_e32 v1, v138, v1
	v_mov_b32_e32 v36, 0
	v_cvt_pk_fp8_f32 v36, v0, v1
	v_add_f32_e32 v30, v32, v76
	v_add_f32_e32 v1, v33, v77
	v_mul_f32_e32 v0, v138, v30
	v_mul_f32_e32 v1, v138, v1
	v_cvt_pk_fp8_f32 v36, v0, v1 op_sel:[0,0,1]
	v_add_f32_e32 v0, v26, v78
	v_add_f32_e32 v1, v27, v79
	v_mul_f32_e32 v0, v138, v0
	v_mul_f32_e32 v1, v138, v1
	v_mov_b32_e32 v37, 0
	v_cvt_pk_fp8_f32 v37, v0, v1
	v_add_f32_e32 v26, v28, v80
	v_add_f32_e32 v1, v29, v81
	v_mul_f32_e32 v0, v138, v26
	v_mul_f32_e32 v1, v138, v1
	v_cvt_pk_fp8_f32 v37, v0, v1 op_sel:[0,0,1]
	v_add_f32_e32 v0, v22, v84
	v_add_f32_e32 v1, v23, v85
	v_mul_f32_e32 v0, v138, v0
	v_mul_f32_e32 v1, v138, v1
	v_mov_b32_e32 v38, 0
	v_cvt_pk_fp8_f32 v38, v0, v1
	v_add_f32_e32 v22, v24, v86
	v_add_f32_e32 v1, v25, v87
	v_mul_f32_e32 v0, v138, v22
	v_mul_f32_e32 v1, v138, v1
	v_cvt_pk_fp8_f32 v38, v0, v1 op_sel:[0,0,1]
	v_add_f32_e32 v0, v14, v66
	v_add_f32_e32 v1, v15, v67
	v_mul_f32_e32 v0, v138, v0
	v_mul_f32_e32 v1, v138, v1
	v_mov_b32_e32 v39, 0
	v_cvt_pk_fp8_f32 v39, v0, v1
	v_add_f32_e32 v14, v16, v68
	v_add_f32_e32 v1, v17, v69
	v_mul_f32_e32 v0, v138, v14
	v_mul_f32_e32 v1, v138, v1
	v_cvt_pk_fp8_f32 v39, v0, v1 op_sel:[0,0,1]
	v_add_f32_e32 v0, v10, v74
	v_add_f32_e32 v1, v11, v75
	v_mul_f32_e32 v0, v138, v0
	v_mul_f32_e32 v1, v138, v1
	v_mov_b32_e32 v32, 0
	v_cvt_pk_fp8_f32 v32, v0, v1
	v_add_f32_e32 v10, v12, v76
	v_add_f32_e32 v1, v13, v77
	v_mul_f32_e32 v0, v138, v10
	v_mul_f32_e32 v1, v138, v1
	v_cvt_pk_fp8_f32 v32, v0, v1 op_sel:[0,0,1]
	v_add_f32_e32 v0, v6, v78
	v_add_f32_e32 v1, v7, v79
	v_mul_f32_e32 v0, v138, v0
	v_mul_f32_e32 v1, v138, v1
	v_mov_b32_e32 v33, 0
	v_cvt_pk_fp8_f32 v33, v0, v1
	v_add_f32_e32 v6, v8, v80
	v_add_f32_e32 v1, v9, v81
	v_mul_f32_e32 v0, v138, v6
	v_mul_f32_e32 v1, v138, v1
	v_cvt_pk_fp8_f32 v33, v0, v1 op_sel:[0,0,1]
	v_add_f32_e32 v0, v2, v84
	v_add_f32_e32 v1, v3, v85
	v_mul_f32_e32 v0, v138, v0
	v_mul_f32_e32 v1, v138, v1
	v_mov_b32_e32 v34, 0
	v_cvt_pk_fp8_f32 v34, v0, v1
	v_add_f32_e32 v2, v4, v86
	v_add_f32_e32 v1, v5, v87
	v_mul_f32_e32 v0, v138, v2
	v_mul_f32_e32 v1, v138, v1
	v_cvt_pk_fp8_f32 v34, v0, v1 op_sel:[0,0,1]
	v_add_f32_e32 v0, v18, v66
	v_add_f32_e32 v1, v19, v67
	v_mov_b32_e32 v35, 0
	v_mul_f32_e32 v0, v138, v0
	v_mul_f32_e32 v1, v138, v1
	v_cvt_pk_fp8_f32 v35, v0, v1
	v_add_f32_e32 v2, v20, v68
	v_add_f32_e32 v1, v21, v69
	v_mul_f32_e32 v0, v138, v2
	v_mul_f32_e32 v1, v138, v1
	v_cvt_pk_fp8_f32 v35, v0, v1 op_sel:[0,0,1]
	v_lshl_add_u64 v[0:1], v[72:73], 0, v[82:83]
	global_store_dwordx4 v[0:1], v[36:39], off sc1
	v_lshl_add_u64 v[0:1], v[72:73], 0, v[70:71]
	global_store_dwordx4 v[0:1], v[32:35], off sc1
	s_endpgm
